# in-proj tail: idle workgroups of the last partial round convert 64 (was 32) weight tiles of the next layer; attention-phase conversion jobs stop earlier (on top of v27)
# baseline (speedup 1.0000x reference)
.LBB0_367:
	s_cmp_eq_u32 s28, 3
	s_cbranch_scc1 .LBB0_486
	s_waitcnt lgkmcnt(0)
	s_mov_b32 s0, s29
	s_cmpk_lg_i32 s0, 0x100
	s_mov_b32 s0, s29
	s_cbranch_scc1 .LBB0_486
	s_abs_i32 s0, s0
	v_cvt_f32_u32_e32 v2, s0
	s_sub_i32 s1, 0, s0
	v_rcp_iflag_f32_e32 v2, v2
	s_nop 0
	v_mul_f32_e32 v2, 0x4f7ffffe, v2
	v_cvt_u32_f32_e32 v2, v2
	s_nop 0
	v_readfirstlane_b32 s9, v2
	s_mul_i32 s1, s1, s9
	s_mul_hi_u32 s1, s9, s1
	s_add_i32 s9, s9, s1
	s_mul_hi_u32 s1, s9, 0x77a
	s_mul_i32 s1, s1, s0
	s_sub_i32 s1, 0x77a, s1
	s_sub_i32 s9, s1, s0
	s_cmp_ge_u32 s1, s0
	s_cselect_b32 s1, s9, s1
	s_sub_i32 s9, s1, s0
	s_cmp_ge_u32 s1, s0
	s_cselect_b32 s0, s9, s1
	v_readlane_b32 s1, v254, 0
	s_mov_b32 s1, s1
	s_cmp_lt_i32 s1, s0
	s_cbranch_scc1 .LBB0_486
	v_readlane_b32 s1, v254, 0
	s_mov_b32 s1, s1
	s_sub_i32 s0, s1, s0
	s_lshl_b32 s59, s0, 6
	s_addk_i32 s59, 0x18b8
	s_nop 0
	v_writelane_b32 v255, s59, 61
	v_writelane_b32 v255, 0, 62
	s_nop 1
.Lfill_pass:
	v_readlane_b32 s59, v255, 61
	v_readlane_b32 s0, v255, 62
	s_nop 3
	s_add_i32 s59, s59, s0
	v_mov_b32 v2, v0
	s_nop 0
	v_readfirstlane_b32 s0, v2
	s_ashr_i32 s0, s0, 6
	s_add_i32 s58, s59, s0
	s_add_i32 s0, s28, 1
	s_add_i32 s59, s59, 32
	s_cmp_lt_i32 s58, s59
	s_cselect_b64 s[30:31], -1, 0
	s_cmp_ge_i32 s58, s59
	s_cbranch_scc1 .LBB0_395
	s_cmpk_gt_i32 s58, 0x72f
	s_mov_b64 s[48:49], -1
	s_cbranch_scc0 .LBB0_392
	s_cmpk_gt_u32 s58, 0x777
	s_mov_b64 s[46:47], -1
	s_cbranch_scc0 .LBB0_389
	s_cmpk_gt_u32 s58, 0x7b7
	s_mov_b64 s[14:15], -1
	s_cbranch_scc0 .LBB0_387
	s_cmpk_gt_u32 s58, 0x937
	s_cbranch_scc0 .LBB0_384
	s_cmpk_gt_u32 s58, 0xa37
	s_cbranch_scc0 .LBB0_381
	s_cmpk_gt_u32 s58, 0x2a37
	s_cbranch_scc0 .LBB0_378
	s_add_i32 s1, s58, 0xffffd5c8
	s_lshr_b32 s70, s1, 8
	s_load_dwordx2 s[14:15], s[76:77], 0xc8
	s_load_dwordx2 s[38:39], s[76:77], 0x118
	s_lshl_b64 s[34:35], s[70:71], 20
	s_lshl_b32 s9, s0, 24
	s_add_u32 s36, s34, s9
	s_addc_u32 s37, s35, 0
	s_lshl_b64 s[34:35], s[36:37], 2
	s_waitcnt lgkmcnt(0)
	s_add_u32 s9, s14, s34
	s_addc_u32 s14, s15, s35
	s_lshl_b32 s15, s1, 2
	s_and_b32 s70, s15, 0x3c0
	s_lshl_b32 s15, s70, 12
	s_add_u32 s9, s9, s15
	s_addc_u32 s14, s14, 0
	s_lshl_b32 s1, s1, 6
	s_and_b32 s1, s1, 0x3c0
	s_lshl_b32 s15, s1, 2
	s_add_u32 s34, s9, s15
	s_addc_u32 s35, s14, 0
	s_lshl_b64 s[14:15], s[36:37], 1
	s_add_u32 s9, s38, s14
	s_addc_u32 s14, s39, s15
	s_lshl_b32 s1, s1, 11
	s_add_u32 s42, s9, s1
	s_addc_u32 s43, s14, 0
	s_mov_b64 s[14:15], 0
	s_mov_b64 s[38:39], s[70:71]

.LBB0_481:
	v_lshlrev_b32_e32 v3, 2, v3
	v_and_b32_e32 v3, 28, v3
	v_mad_i64_i32 v[4:5], s[0:1], v3, s46, 0
	s_ashr_i32 s47, s46, 31
	v_lshl_add_u64 v[4:5], v[4:5], 1, s[50:51]
	v_lshlrev_b32_e32 v194, 1, v2
	v_lshl_add_u64 v[6:7], v[4:5], 0, v[194:195]
	s_lshl_b64 s[0:1], s[46:47], 1
	v_cvt_pk_bf16_f32 v2, v126, v94
	v_cvt_pk_bf16_f32 v3, v98, v106
	v_cvt_pk_bf16_f32 v4, v110, v114
	v_cvt_pk_bf16_f32 v5, v118, v122
	global_store_dwordx4 v[6:7], v[2:5], off nt
	v_lshl_add_u64 v[6:7], v[6:7], 0, s[0:1]
	s_nop 0
	v_cvt_pk_bf16_f32 v2, v127, v95
	v_cvt_pk_bf16_f32 v3, v99, v107
	v_cvt_pk_bf16_f32 v4, v111, v115
	v_cvt_pk_bf16_f32 v5, v119, v123
	global_store_dwordx4 v[6:7], v[2:5], off nt
	v_lshl_add_u64 v[6:7], v[6:7], 0, s[0:1]
	s_nop 0
	v_cvt_pk_bf16_f32 v2, v128, v96
	v_cvt_pk_bf16_f32 v3, v100, v108
	v_cvt_pk_bf16_f32 v4, v112, v116
	v_cvt_pk_bf16_f32 v5, v120, v124
	global_store_dwordx4 v[6:7], v[2:5], off nt
	v_lshl_add_u64 v[6:7], v[6:7], 0, s[0:1]
	s_nop 0
	v_cvt_pk_bf16_f32 v2, v129, v97
	v_cvt_pk_bf16_f32 v3, v101, v109
	v_cvt_pk_bf16_f32 v4, v113, v117
	v_cvt_pk_bf16_f32 v5, v121, v125
	global_store_dwordx4 v[6:7], v[2:5], off nt
	v_mad_i64_i32 v[6:7], s[14:15], s46, 58, v[6:7]
	s_nop 0
	v_cvt_pk_bf16_f32 v2, v66, v70
	v_cvt_pk_bf16_f32 v3, v74, v78
	v_cvt_pk_bf16_f32 v4, v82, v86
	v_cvt_pk_bf16_f32 v5, v90, v102
	global_store_dwordx4 v[6:7], v[2:5], off nt
	v_lshl_add_u64 v[6:7], v[6:7], 0, s[0:1]
	s_nop 0
	v_cvt_pk_bf16_f32 v2, v67, v71
	v_cvt_pk_bf16_f32 v3, v75, v79
	v_cvt_pk_bf16_f32 v4, v83, v87
	v_cvt_pk_bf16_f32 v5, v91, v103
	global_store_dwordx4 v[6:7], v[2:5], off nt
	v_lshl_add_u64 v[6:7], v[6:7], 0, s[0:1]
	s_nop 0
	v_cvt_pk_bf16_f32 v2, v68, v72
	v_cvt_pk_bf16_f32 v3, v76, v80
	v_cvt_pk_bf16_f32 v4, v84, v88
	v_cvt_pk_bf16_f32 v5, v92, v104
	global_store_dwordx4 v[6:7], v[2:5], off nt
	v_lshl_add_u64 v[6:7], v[6:7], 0, s[0:1]
	s_nop 0
	v_cvt_pk_bf16_f32 v2, v69, v73
	v_cvt_pk_bf16_f32 v3, v77, v81
	v_cvt_pk_bf16_f32 v4, v85, v89
	v_cvt_pk_bf16_f32 v5, v93, v105
	global_store_dwordx4 v[6:7], v[2:5], off nt
	s_branch .Lfill_next

.Lfill_next:
	v_readlane_b32 s0, v255, 62
	s_nop 3
	s_add_i32 s0, s0, 32
	s_cmpk_ge_i32 s0, 0x40
	s_cbranch_scc1 .LBB0_486
	s_nop 0
	v_writelane_b32 v255, s0, 62
	s_nop 1
	s_branch .Lfill_pass

.LBB0_827:
	s_andn2_b64 vcc, exec, s[46:47]
	s_cbranch_vccnz .LBB0_940
	s_mul_hi_i32 s0, s9, 0x2e8ba2e9
	s_lshr_b32 s1, s0, 31
	s_ashr_i32 s0, s0, 1
	s_add_i32 s0, s0, s1
	s_mul_i32 s1, s0, -11
	s_add_i32 s1, s1, s9
	s_cmp_lt_i32 s1, 9
	s_cbranch_scc1 .LBB0_940
	s_lshl_b32 s0, s0, 1
	s_add_i32 s0, s0, s1
	s_add_i32 s0, s0, -9
	s_cmpk_gt_i32 s0, 0x1d1
	s_cbranch_scc1 .LBB0_940
	v_readlane_b32 s14, v254, 3
	v_readlane_b32 s15, v254, 4
	s_load_dword s1, s[14:15], 0x0
	s_waitcnt lgkmcnt(0)
	s_mov_b32 s1, s1
	s_cmpk_eq_i32 s1, 0x100
	s_movk_i32 s1, 0x3a38
	s_cselect_b32 s1, 0x18b8, s1
	s_lshl_b32 s0, s0, 5
	s_cmp_le_i32 s1, s0
	s_cbranch_scc1 .LBB0_940
	s_add_i32 s9, s0, 32
	s_min_i32 s52, s9, s1
	v_mov_b32 v2, v0
	s_nop 0
	v_readfirstlane_b32 s1, v2
	s_ashr_i32 s59, s1, 6
	s_add_i32 s59, s59, s0
	s_cmp_lt_i32 s59, s52
	s_cselect_b64 s[86:87], -1, 0
	s_cmp_ge_i32 s59, s52
	s_cbranch_scc1 .LBB0_856
	s_cmpk_gt_i32 s59, 0x72f
	s_mov_b64 s[42:43], -1
	s_cbranch_scc0 .LBB0_853
	s_cmpk_gt_u32 s59, 0x777
	s_cbranch_scc0 .LBB0_850
	s_cmpk_gt_u32 s59, 0x7b7
	s_mov_b64 s[14:15], -1
	s_cbranch_scc0 .LBB0_848
	s_cmpk_gt_u32 s59, 0x937
	s_mov_b64 s[0:1], -1
	s_cbranch_scc0 .LBB0_845
	s_cmpk_gt_u32 s59, 0xa37
	s_cbranch_scc0 .LBB0_842
	s_cmpk_gt_u32 s59, 0x2a37
	s_cbranch_scc0 .LBB0_839
	s_add_i32 s9, s59, 0xffffd5c8
	s_lshr_b32 s70, s9, 8
	s_load_dwordx2 s[0:1], s[76:77], 0xc8
	s_load_dwordx2 s[34:35], s[76:77], 0x118
	s_lshl_b64 s[14:15], s[70:71], 20
	s_add_u32 s14, s14, s62
	s_addc_u32 s15, s15, s63
	s_lshl_b64 s[30:31], s[14:15], 2
	s_waitcnt lgkmcnt(0)
	s_add_u32 s0, s0, s30
	s_addc_u32 s1, s1, s31
	s_lshl_b32 s30, s9, 2
	s_and_b32 s70, s30, 0x3c0
	s_lshl_b32 s30, s70, 12
	s_add_u32 s0, s0, s30
	s_addc_u32 s1, s1, 0
	s_lshl_b32 s9, s9, 6
	s_and_b32 s9, s9, 0x3c0
	s_lshl_b32 s30, s9, 2
	s_add_u32 s30, s0, s30
	s_addc_u32 s31, s1, 0
	s_lshl_b64 s[0:1], s[14:15], 1
	s_add_u32 s0, s34, s0
	s_addc_u32 s1, s35, s1
	s_lshl_b32 s9, s9, 11
	s_add_u32 s34, s0, s9
	s_addc_u32 s35, s1, 0
	s_mov_b64 s[0:1], 0
	s_mov_b64 s[38:39], s[70:71]
